# deferred weight-conversion split: all layer-1 tiles deferred, balanced idle-slot quotas 6/6/6/6, remainder converted by the catch-all
# baseline (speedup 1.0000x reference)
; #define SEAM(k) do { if (IN(k) && IN((k) + 1)) xcd_barrier(bar); \
;         if (PROBE_MASK) { const unsigned long long t_ = __builtin_amdgcn_s_memrealtime(); if ((PROBE_MASK >> (k)) & 1u) pr_acc += t_ - pr_t0; pr_t0 = t_; } } while (0)
; __device__ __forceinline__ void convert_deferred(const Ptrs& P, unsigned char* lds, int quota) {
;     const int tid = threadIdx.x, wid = tid >> 6, lane = tid & 63;
;     float* tile = (float*)lds;
;     volatile __attribute__((address_space(3))) int* slot = (volatile __attribute__((address_space(3))) int*)((__attribute__((address_space(3))) unsigned char*)lds + 131072 + 320 + 11000);
;     unsigned* q = (unsigned*)(P.ws + WS_CTL) + CW_DEFQ;
;     for (int n = 0; n < quota; ++n) {
;         __syncthreads();
;         if (tid == 0) *slot = (int)atomicAdd(q, 1u);
;         __syncthreads();
;         const int t = *slot;
;         if (t >= DEF_GU + DEF_DN) break;
;         const bool gu = t < DEF_GU;
;         const float* src = gu ? P.in[34] : P.in[36]; bf16* dst = (bf16*)(P.ws + (gu ? WS_WGU : WS_WDN));
;         const int N = gu ? 2048 : 1024, ntn = N / 256, it = gu ? 2 * NE * 16 * 8 - DEF_GU + t : 2 * NE * 16 * 4 - DEF_DN + (t - DEF_GU);
; __global__ void __launch_bounds__(NT, 2) mega(Args args) {
;     ...
;         if (IDLE_LAST(68 * 4)) convert_deferred(P, lds, 4); } SEAM(6);
.LBB0_1286:
	s_abs_i32 s3, s62
	v_cvt_f32_u32_e32 v2, s3
	s_sub_i32 s4, 0, s3
	s_mov_b32 s5, 0
	v_rcp_iflag_f32_e32 v2, v2
	s_nop 0
	v_mul_f32_e32 v2, 0x4f7ffffe, v2
	v_cvt_u32_f32_e32 v2, v2
	s_nop 0
	v_readfirstlane_b32 s6, v2
	s_mul_i32 s4, s4, s6
	s_mul_hi_u32 s4, s6, s4
	s_add_i32 s6, s6, s4
	s_mul_hi_u32 s4, s6, 0x110
	s_mul_i32 s4, s4, s3
	s_sub_i32 s4, 0x110, s4
	s_sub_i32 s6, s4, s3
	s_cmp_ge_u32 s4, s3
	s_cselect_b32 s4, s6, s4
	s_sub_i32 s6, s4, s3
	s_cmp_ge_u32 s4, s3
	s_cselect_b32 s3, s6, s4
	s_cmp_eq_u32 s3, 0
	s_cselect_b64 s[6:7], -1, 0
	s_cmp_lt_i32 s2, s3
	s_cselect_b64 s[8:9], -1, 0
	s_or_b64 s[6:7], s[6:7], s[8:9]
	s_and_b64 vcc, exec, s[6:7]
	s_cbranch_vccnz .LBB0_1296
	v_and_b32_e32 v2, 0x7c, v188
	v_lshlrev_b32_e32 v3, 5, v0
	s_movk_i32 s3, 0x400
	v_and_or_b32 v12, v3, s3, v2
	v_bfe_u32 v2, v0, 3, 3
	v_lshl_or_b32 v4, v1, 5, v2
	v_lshlrev_b32_e32 v2, 3, v0
	v_lshl_add_u32 v11, v182, 4, 0
	v_and_b32_e32 v2, 56, v2
	v_mul_u32_u24_e32 v16, 0x2020, v1
	v_mov_b32_e32 v3, 0
	v_lshl_add_u32 v27, v4, 2, 0
	v_mul_u32_u24_e32 v28, 0x404, v2
	v_lshlrev_b32_e32 v10, 6, v4
	s_add_i32 s12, 0, 0x22c38
	v_add_u32_e32 v16, v11, v16
	v_and_b32_e32 v13, 0xfc, v188
	v_and_b32_e32 v14, 56, v185
	s_mov_b32 s3, 6
	v_or_b32_e32 v4, 0x200, v10
	v_mov_b32_e32 v5, v3
	v_or_b32_e32 v6, 0x400, v10
	v_mov_b32_e32 v7, v3
	v_or_b32_e32 v8, 0x600, v10
	v_mov_b32_e32 v9, v3
	v_mov_b32_e32 v15, s12
	s_movk_i32 s13, 0x17ff
	s_movk_i32 s14, 0x800
	s_mov_b32 s15, 0x1104e000
	s_movk_i32 s16, -2048
	v_add_u32_e32 v17, 0x404, v16
	v_add_u32_e32 v18, 0x40c, v16
	v_add_u32_e32 v19, 0x808, v16
	v_add_u32_e32 v20, 0xc0c, v16
	v_add_u32_e32 v21, 0xc14, v16
	v_add_u32_e32 v22, 0x1414, v16
	v_add_u32_e32 v23, 0x141c, v16
	v_add_u32_e32 v24, 0x1818, v16
	v_add_u32_e32 v25, 0x1c1c, v16
	v_add_u32_e32 v26, 0x1c24, v16
	v_lshlrev_b32_e32 v2, 1, v2
	v_add_u32_e32 v27, v27, v28
	v_lshlrev_b32_e32 v10, 1, v10
	s_branch .LBB0_1289

; #define LAS __attribute__((address_space(3)))
; #define SEAM(k) do { if (IN(k) && IN((k) + 1)) xcd_barrier(bar); \
;         if (PROBE_MASK) { const unsigned long long t_ = __builtin_amdgcn_s_memrealtime(); if ((PROBE_MASK >> (k)) & 1u) pr_acc += t_ - pr_t0; pr_t0 = t_; } } while (0)
; __device__ __forceinline__ void convert_deferred(const Ptrs& P, unsigned char* lds, int quota) {
;     const int tid = threadIdx.x, wid = tid >> 6, lane = tid & 63;
;     float* tile = (float*)lds;
;     volatile __attribute__((address_space(3))) int* slot = (volatile __attribute__((address_space(3))) int*)((__attribute__((address_space(3))) unsigned char*)lds + 131072 + 320 + 11000);
;     unsigned* q = (unsigned*)(P.ws + WS_CTL) + CW_DEFQ;
;     for (int n = 0; n < quota; ++n) {
;         __syncthreads();
;         if (tid == 0) *slot = (int)atomicAdd(q, 1u);
;         __syncthreads();
;         const int t = *slot;
;         if (t >= DEF_GU + DEF_DN) break;
;         const bool gu = t < DEF_GU;
;         const float* src = gu ? P.in[34] : P.in[36]; bf16* dst = (bf16*)(P.ws + (gu ? WS_WGU : WS_WDN));
;         const int N = gu ? 2048 : 1024, ntn = N / 256, it = gu ? 2 * NE * 16 * 8 - DEF_GU + t : 2 * NE * 16 * 4 - DEF_DN + (t - DEF_GU);
; __global__ void __launch_bounds__(NT, 2) mega(Args args) {
;     ...
;         { const int rem_ = ((LAS int*)(LDSP + MISC_OFF + 256))[96] % G; if (rem_ != 0 && vcu >= rem_) convert_deferred(P, lds, 5); } } SEAM(9);
.LBB0_1609:
	s_abs_i32 s0, s62
	v_cvt_f32_u32_e32 v2, s0
	s_sub_i32 s5, 0, s0
	s_abs_i32 s4, s9
	s_ashr_i32 s3, s9, 31
	v_rcp_iflag_f32_e32 v2, v2
	s_mov_b32 s1, 0
	v_mul_f32_e32 v2, 0x4f7ffffe, v2
	v_cvt_u32_f32_e32 v2, v2
	s_nop 0
	v_readfirstlane_b32 s6, v2
	s_mul_i32 s5, s5, s6
	s_mul_hi_u32 s5, s6, s5
	s_add_i32 s6, s6, s5
	s_mul_hi_u32 s5, s4, s6
	s_mul_i32 s5, s5, s0
	s_sub_i32 s4, s4, s5
	s_sub_i32 s5, s4, s0
	s_cmp_ge_u32 s4, s0
	s_cselect_b32 s4, s5, s4
	s_sub_i32 s5, s4, s0
	s_cmp_ge_u32 s4, s0
	s_cselect_b32 s0, s5, s4
	s_xor_b32 s0, s0, s3
	s_sub_i32 s0, s0, s3
	s_cmp_eq_u32 s0, 0
	v_readlane_b32 s3, v254, 2
	s_cselect_b64 s[4:5], -1, 0
	s_cmp_lt_i32 s3, s0
	s_cselect_b64 s[6:7], -1, 0
	s_or_b64 s[4:5], s[4:5], s[6:7]
	s_and_b64 vcc, exec, s[4:5]
	s_cbranch_vccnz .LBB0_1619
	v_and_b32_e32 v2, 0x7c, v175
	v_lshlrev_b32_e32 v3, 5, v0
	s_movk_i32 s0, 0x400
	v_and_or_b32 v12, v3, s0, v2
	v_bfe_u32 v2, v0, 3, 3
	v_lshl_or_b32 v4, v1, 5, v2
	v_lshlrev_b32_e32 v2, 3, v0
	v_lshl_add_u32 v11, v182, 4, 0
	v_and_b32_e32 v2, 56, v2
	v_mul_u32_u24_e32 v16, 0x2020, v1
	v_mov_b32_e32 v3, 0
	v_lshl_add_u32 v27, v4, 2, 0
	v_mul_u32_u24_e32 v28, 0x404, v2
	v_lshlrev_b32_e32 v10, 6, v4
	s_add_i32 s10, 0, 0x22c38
	v_add_u32_e32 v16, v11, v16
	s_mov_b32 s3, 6
	v_and_b32_e32 v13, 0xfc, v175
	v_and_b32_e32 v14, 56, v173
	v_or_b32_e32 v4, 0x200, v10
	v_mov_b32_e32 v5, v3
	v_or_b32_e32 v6, 0x400, v10
	v_mov_b32_e32 v7, v3
	v_or_b32_e32 v8, 0x600, v10
	v_mov_b32_e32 v9, v3
	v_mov_b32_e32 v15, s10
	s_movk_i32 s11, 0x17ff
	s_movk_i32 s12, 0x800
	s_mov_b32 s13, 0x1104e000
	s_movk_i32 s14, -2048
	v_add_u32_e32 v17, 0x404, v16
	v_add_u32_e32 v18, 0x40c, v16
	v_add_u32_e32 v19, 0x808, v16
	v_add_u32_e32 v20, 0xc0c, v16
	v_add_u32_e32 v21, 0xc14, v16
	v_add_u32_e32 v22, 0x1414, v16
	v_add_u32_e32 v23, 0x141c, v16
	v_add_u32_e32 v24, 0x1818, v16
	v_add_u32_e32 v25, 0x1c1c, v16
	v_add_u32_e32 v26, 0x1c24, v16
	v_lshlrev_b32_e32 v2, 1, v2
	v_add_u32_e32 v27, v27, v28
	v_lshlrev_b32_e32 v10, 1, v10
	s_branch .LBB0_1612

; #define SEAM(k) do { if (IN(k) && IN((k) + 1)) xcd_barrier(bar); \
;         if (PROBE_MASK) { const unsigned long long t_ = __builtin_amdgcn_s_memrealtime(); if ((PROBE_MASK >> (k)) & 1u) pr_acc += t_ - pr_t0; pr_t0 = t_; } } while (0)
; __device__ __forceinline__ void convert_deferred(const Ptrs& P, unsigned char* lds, int quota) {
;     const int tid = threadIdx.x, wid = tid >> 6, lane = tid & 63;
;     float* tile = (float*)lds;
;     volatile __attribute__((address_space(3))) int* slot = (volatile __attribute__((address_space(3))) int*)((__attribute__((address_space(3))) unsigned char*)lds + 131072 + 320 + 11000);
;     unsigned* q = (unsigned*)(P.ws + WS_CTL) + CW_DEFQ;
;     for (int n = 0; n < quota; ++n) {
;         __syncthreads();
;         if (tid == 0) *slot = (int)atomicAdd(q, 1u);
;         __syncthreads();
;         const int t = *slot;
;         if (t >= DEF_GU + DEF_DN) break;
;         const bool gu = t < DEF_GU;
;         const float* src = gu ? P.in[34] : P.in[36]; bf16* dst = (bf16*)(P.ws + (gu ? WS_WGU : WS_WDN));
;         const int N = gu ? 2048 : 1024, ntn = N / 256, it = gu ? 2 * NE * 16 * 8 - DEF_GU + t : 2 * NE * 16 * 4 - DEF_DN + (t - DEF_GU);
; __global__ void __launch_bounds__(NT, 2) mega(Args args) {
;     ...
;         if (IDLE_LAST(68 * 12)) convert_deferred(P, lds, 4); } SEAM(11);
.LBB0_1851:
	s_abs_i32 s0, s62
	v_cvt_f32_u32_e32 v2, s0
	s_sub_i32 s3, 0, s0
	v_readlane_b32 s56, v254, 40
	s_mov_b32 s1, 0
	v_rcp_iflag_f32_e32 v2, v2
	v_readlane_b32 s57, v254, 41
	v_mul_f32_e32 v2, 0x4f7ffffe, v2
	v_cvt_u32_f32_e32 v2, v2
	s_nop 0
	v_readfirstlane_b32 s4, v2
	s_mul_i32 s3, s3, s4
	s_mul_hi_u32 s3, s4, s3
	s_add_i32 s4, s4, s3
	s_mul_hi_u32 s3, s4, 0x330
	s_mul_i32 s3, s3, s0
	s_sub_i32 s3, 0x330, s3
	s_sub_i32 s4, s3, s0
	s_cmp_ge_u32 s3, s0
	s_cselect_b32 s3, s4, s3
	s_sub_i32 s4, s3, s0
	s_cmp_ge_u32 s3, s0
	s_cselect_b32 s0, s4, s3
	s_cmp_eq_u32 s0, 0
	s_cselect_b64 s[4:5], -1, 0
	s_cmp_lt_i32 s2, s0
	s_cselect_b64 s[6:7], -1, 0
	s_or_b64 s[4:5], s[4:5], s[6:7]
	s_and_b64 vcc, exec, s[4:5]
	s_cbranch_vccnz .LBB0_1861
	v_and_b32_e32 v2, 0x7c, v218
	v_lshlrev_b32_e32 v3, 5, v0
	s_movk_i32 s0, 0x400
	v_and_or_b32 v12, v3, s0, v2
	v_bfe_u32 v2, v0, 3, 3
	v_lshl_or_b32 v4, v1, 5, v2
	v_lshlrev_b32_e32 v2, 3, v0
	v_lshl_add_u32 v11, v182, 4, 0
	v_and_b32_e32 v2, 56, v2
	v_mul_u32_u24_e32 v16, 0x2020, v1
	v_mov_b32_e32 v3, 0
	s_waitcnt vmcnt(0)
	v_lshl_add_u32 v27, v4, 2, 0
	v_mul_u32_u24_e32 v28, 0x404, v2
	v_lshlrev_b32_e32 v10, 6, v4
	s_add_i32 s10, 0, 0x22c38
	v_add_u32_e32 v16, v11, v16
	v_and_b32_e32 v13, 0xfc, v218
	v_and_b32_e32 v14, 56, v179
	s_mov_b32 s3, 6
	v_or_b32_e32 v4, 0x200, v10
	v_mov_b32_e32 v5, v3
	v_or_b32_e32 v6, 0x400, v10
	v_mov_b32_e32 v7, v3
	v_or_b32_e32 v8, 0x600, v10
	v_mov_b32_e32 v9, v3
	v_mov_b32_e32 v15, s10
	s_movk_i32 s11, 0x17ff
	s_movk_i32 s12, 0x800
	s_mov_b32 s13, 0x1104e000
	s_movk_i32 s14, -2048
	v_add_u32_e32 v17, 0x404, v16
	v_add_u32_e32 v18, 0x40c, v16
	v_add_u32_e32 v19, 0x808, v16
	v_add_u32_e32 v20, 0xc0c, v16
	v_add_u32_e32 v21, 0xc14, v16
	v_add_u32_e32 v22, 0x1414, v16
	v_add_u32_e32 v23, 0x141c, v16
	v_add_u32_e32 v24, 0x1818, v16
	v_add_u32_e32 v25, 0x1c1c, v16
	v_add_u32_e32 v26, 0x1c24, v16
	v_lshlrev_b32_e32 v2, 1, v2
	v_add_u32_e32 v27, v27, v28
	v_lshlrev_b32_e32 v10, 1, v10
	s_branch .LBB0_1854
